# adds: stick-breaking loop body without diagonal-mask selects for non-diagonal tiles; DSA indexer relu without canonicalising v_max
# baseline (speedup 1.0000x reference)
.LBB0_536:
	s_add_u32 s19, s8, s12
	v_or_b32_e32 v32, s19, v66
	v_mov_b64_e32 v[36:37], s[88:89]
	s_addc_u32 s24, s9, 0
	v_mad_u64_u32 v[32:33], s[20:21], v32, s10, v[36:37]
	v_mad_i32_i24 v33, s24, v241, v33
	v_lshl_add_u64 v[32:33], v[32:33], 0, s[26:27]
	v_mov_b32_e32 v71, v48
	v_lshl_add_u64 v[32:33], v[32:33], 0, v[70:71]
	s_mov_b64 s[20:21], 0x1b80
	v_lshl_add_u64 v[38:39], v[32:33], 0, s[20:21]
	v_add_co_u32_e32 v32, vcc, s16, v32
	v_mov_b32_e32 v73, v48
	s_nop 0
	v_addc_co_u32_e32 v33, vcc, 0, v33, vcc
	global_load_dwordx4 v[32:35], v[32:33], off offset:2944
	s_nop 0
	global_load_dwordx4 v[78:81], v[38:39], off offset:32
	global_load_dwordx4 v[82:85], v[38:39], off offset:64
	global_load_dwordx4 v[86:89], v[38:39], off offset:96
	v_or_b32_e32 v38, s19, v68
	v_mad_u64_u32 v[36:37], s[20:21], v38, s10, v[36:37]
	v_mad_i32_i24 v37, s24, v241, v37
	v_lshl_add_u64 v[36:37], v[36:37], 0, s[26:27]
	v_lshl_add_u64 v[90:91], v[36:37], 0, v[72:73]
	v_add_co_u32_e32 v36, vcc, s16, v90
	s_mov_b32 s19, 0x13000
	s_nop 0
	v_addc_co_u32_e32 v37, vcc, 0, v91, vcc
	v_add_co_u32_e32 v40, vcc, s19, v90
	s_mov_b32 s19, 0x25000
	s_nop 0
	v_addc_co_u32_e32 v41, vcc, 0, v91, vcc
	v_add_co_u32_e32 v44, vcc, s19, v90
	global_load_dwordx4 v[36:39], v[36:37], off offset:3968
	s_nop 0
	v_addc_co_u32_e32 v45, vcc, 0, v91, vcc
	s_mov_b32 s19, 0x37000
	global_load_dwordx4 v[40:43], v[40:41], off offset:3968
	v_add_co_u32_e32 v90, vcc, s19, v90
	global_load_dwordx4 v[44:47], v[44:45], off offset:3968
	s_nop 0
	v_addc_co_u32_e32 v91, vcc, 0, v91, vcc
	global_load_dwordx4 v[90:93], v[90:91], off offset:3968
	s_cmp_eq_u32 s18, 0
	s_cselect_b64 vcc, -1, 0
	s_mov_b32 s19, 0xda24260
	s_waitcnt vmcnt(3)
	ds_write_b128 v76, v[36:39]
	s_waitcnt vmcnt(2)
	ds_write_b128 v76, v[40:43] offset:1152
	s_waitcnt vmcnt(1)
	ds_write_b128 v76, v[44:47] offset:2304
	s_waitcnt vmcnt(0)
	ds_write_b128 v76, v[90:93] offset:3456
	v_mfma_f32_32x32x16_bf16 v[32:47], v[32:35], v[58:61], 0
	s_waitcnt lgkmcnt(0)
	v_mfma_f32_32x32x16_bf16 v[32:47], v[78:81], v[50:53], v[32:47]
	v_mfma_f32_32x32x16_bf16 v[32:47], v[82:85], v[54:57], v[32:47]
	v_mfma_f32_32x32x16_bf16 v[32:47], v[86:89], v[62:65], v[32:47]
	s_nop 11
	v_mul_f32_e32 v47, 0xbe38aa3b, v47
	v_min_f32_e32 v47, 0x42e60000, v47
	v_exp_f32_e32 v47, v47
	v_mul_f32_e32 v46, 0xbe38aa3b, v46
	v_min_f32_e32 v46, 0x42e60000, v46
	v_exp_f32_e32 v46, v46
	v_add_f32_e32 v71, 1.0, v47
	v_rcp_f32_e32 v71, v71
	v_mul_f32_e32 v45, 0xbe38aa3b, v45
	v_min_f32_e32 v45, 0x42e60000, v45
	v_exp_f32_e32 v45, v45
	v_mul_f32_e32 v47, v47, v71
	v_cndmask_b32_e64 v73, 1.0, v47, s[40:41]
	v_cndmask_b32_e64 v77, 0, v71, s[40:41]
	v_cndmask_b32_e32 v73, v47, v73, vcc
	v_cndmask_b32_e32 v47, v71, v77, vcc
	v_add_f32_e32 v71, 1.0, v46
	v_rcp_f32_e32 v71, v71
	v_mul_f32_e32 v44, 0xbe38aa3b, v44
	v_min_f32_e32 v44, 0x42e60000, v44
	v_exp_f32_e32 v44, v44
	v_mul_f32_e32 v46, v46, v71
	v_cndmask_b32_e64 v77, 1.0, v46, s[42:43]
	v_cndmask_b32_e64 v78, 0, v71, s[42:43]
	v_cndmask_b32_e32 v77, v46, v77, vcc
	v_cndmask_b32_e32 v46, v71, v78, vcc
	v_mul_f32_e32 v46, v46, v73
	v_mul_f32_e32 v71, v73, v77
	v_add_f32_e32 v73, 1.0, v45
	v_rcp_f32_e32 v73, v73
	v_mul_f32_e32 v43, 0xbe38aa3b, v43
	v_min_f32_e32 v43, 0x42e60000, v43
	v_exp_f32_e32 v43, v43
	v_mul_f32_e32 v45, v45, v73
	v_cndmask_b32_e64 v77, 1.0, v45, s[44:45]
	v_cndmask_b32_e64 v78, 0, v73, s[44:45]
	v_cndmask_b32_e32 v45, v45, v77, vcc
	v_cndmask_b32_e32 v73, v73, v78, vcc
	v_mul_f32_e32 v73, v73, v71
	v_mul_f32_e32 v45, v45, v71
	v_add_f32_e32 v71, 1.0, v44
	v_rcp_f32_e32 v71, v71
	v_mul_f32_e32 v42, 0xbe38aa3b, v42
	v_min_f32_e32 v42, 0x42e60000, v42
	v_exp_f32_e32 v42, v42
	v_mul_f32_e32 v44, v44, v71
	v_cndmask_b32_e64 v77, 1.0, v44, s[46:47]
	v_cndmask_b32_e64 v78, 0, v71, s[46:47]
	v_cndmask_b32_e32 v44, v44, v77, vcc
	v_cndmask_b32_e32 v71, v71, v78, vcc
	v_mul_f32_e32 v71, v71, v45
	v_mul_f32_e32 v44, v44, v45
	v_add_f32_e32 v45, 1.0, v43
	v_rcp_f32_e32 v45, v45
	v_mul_f32_e32 v41, 0xbe38aa3b, v41
	v_min_f32_e32 v41, 0x42e60000, v41
	v_exp_f32_e32 v41, v41
	v_mul_f32_e32 v43, v43, v45
	v_cndmask_b32_e64 v77, 1.0, v43, s[48:49]
	v_cndmask_b32_e64 v78, 0, v45, s[48:49]
	v_cndmask_b32_e32 v43, v43, v77, vcc
	v_cndmask_b32_e32 v45, v45, v78, vcc
	v_mul_f32_e32 v45, v45, v44
	v_mul_f32_e32 v43, v43, v44
	v_add_f32_e32 v44, 1.0, v42
	v_rcp_f32_e32 v44, v44
	v_mul_f32_e32 v40, 0xbe38aa3b, v40
	v_min_f32_e32 v40, 0x42e60000, v40
	v_exp_f32_e32 v40, v40
	v_mul_f32_e32 v42, v42, v44
	v_cndmask_b32_e64 v77, 1.0, v42, s[50:51]
	v_cndmask_b32_e64 v78, 0, v44, s[50:51]
	v_cndmask_b32_e32 v42, v42, v77, vcc
	v_cndmask_b32_e32 v44, v44, v78, vcc
	v_mul_f32_e32 v44, v44, v43
	v_mul_f32_e32 v42, v42, v43
	v_add_f32_e32 v43, 1.0, v41
	v_rcp_f32_e32 v43, v43
	v_mul_f32_e32 v39, 0xbe38aa3b, v39
	v_min_f32_e32 v39, 0x42e60000, v39
	v_exp_f32_e32 v39, v39
	v_mul_f32_e32 v41, v41, v43
	v_cndmask_b32_e64 v77, 1.0, v41, s[52:53]
	v_cndmask_b32_e64 v78, 0, v43, s[52:53]
	v_cndmask_b32_e32 v41, v41, v77, vcc
	v_cndmask_b32_e32 v43, v43, v78, vcc
	v_mul_f32_e32 v43, v43, v42
	v_mul_f32_e32 v41, v41, v42
	v_add_f32_e32 v42, 1.0, v40
	v_rcp_f32_e32 v42, v42
	v_mul_f32_e32 v38, 0xbe38aa3b, v38
	v_min_f32_e32 v38, 0x42e60000, v38
	v_exp_f32_e32 v38, v38
	v_mul_f32_e32 v40, v40, v42
	v_cndmask_b32_e64 v77, 1.0, v40, s[54:55]
	v_cndmask_b32_e64 v78, 0, v42, s[54:55]
	v_cndmask_b32_e32 v40, v40, v77, vcc
	v_cndmask_b32_e32 v42, v42, v78, vcc
	v_mul_f32_e32 v42, v42, v41
	v_mul_f32_e32 v40, v40, v41
	v_add_f32_e32 v41, 1.0, v39
	v_rcp_f32_e32 v41, v41
	v_mul_f32_e32 v37, 0xbe38aa3b, v37
	v_min_f32_e32 v37, 0x42e60000, v37
	v_exp_f32_e32 v37, v37
	v_mul_f32_e32 v39, v39, v41
	v_cndmask_b32_e64 v77, 1.0, v39, s[56:57]
	v_cndmask_b32_e64 v78, 0, v41, s[56:57]
	v_cndmask_b32_e32 v39, v39, v77, vcc
	v_cndmask_b32_e32 v41, v41, v78, vcc
	v_mul_f32_e32 v41, v41, v40
	v_mul_f32_e32 v39, v39, v40
	v_add_f32_e32 v40, 1.0, v38
	v_rcp_f32_e32 v40, v40
	v_mul_f32_e32 v36, 0xbe38aa3b, v36
	v_min_f32_e32 v36, 0x42e60000, v36
	v_exp_f32_e32 v36, v36
	v_mul_f32_e32 v38, v38, v40
	v_cndmask_b32_e64 v77, 1.0, v38, s[58:59]
	v_cndmask_b32_e64 v78, 0, v40, s[58:59]
	v_cndmask_b32_e32 v38, v38, v77, vcc
	v_cndmask_b32_e32 v40, v40, v78, vcc
	v_mul_f32_e32 v77, v40, v39
	v_mul_f32_e32 v38, v38, v39
	v_add_f32_e32 v39, 1.0, v37
	v_rcp_f32_e32 v39, v39
	v_mul_f32_e32 v35, 0xbe38aa3b, v35
	v_min_f32_e32 v35, 0x42e60000, v35
	v_exp_f32_e32 v35, v35
	v_mul_f32_e32 v37, v37, v39
	v_cndmask_b32_e64 v40, 1.0, v37, s[60:61]
	v_cndmask_b32_e64 v78, 0, v39, s[60:61]
	v_cndmask_b32_e32 v37, v37, v40, vcc
	v_cndmask_b32_e32 v39, v39, v78, vcc
	v_mul_f32_e32 v39, v39, v38
	v_mul_f32_e32 v37, v37, v38
	v_add_f32_e32 v38, 1.0, v36
	v_rcp_f32_e32 v38, v38
	v_mul_f32_e32 v34, 0xbe38aa3b, v34
	v_min_f32_e32 v34, 0x42e60000, v34
	v_exp_f32_e32 v34, v34
	v_mul_f32_e32 v36, v36, v38
	v_cndmask_b32_e64 v40, 1.0, v36, s[62:63]
	v_cndmask_b32_e64 v78, 0, v38, s[62:63]
	v_cndmask_b32_e32 v36, v36, v40, vcc
	v_cndmask_b32_e32 v38, v38, v78, vcc
	v_mul_f32_e32 v38, v38, v37
	v_mul_f32_e32 v36, v36, v37
	v_add_f32_e32 v37, 1.0, v35
	v_rcp_f32_e32 v37, v37
	v_mul_f32_e32 v33, 0xbe38aa3b, v33
	v_min_f32_e32 v33, 0x42e60000, v33
	v_exp_f32_e32 v33, v33
	v_mul_f32_e32 v35, v35, v37
	v_cndmask_b32_e64 v40, 1.0, v35, s[64:65]
	v_cndmask_b32_e64 v78, 0, v37, s[64:65]
	v_cndmask_b32_e32 v35, v35, v40, vcc
	v_cndmask_b32_e32 v37, v37, v78, vcc
	v_mul_f32_e32 v37, v37, v36
	v_mul_f32_e32 v35, v35, v36
	v_add_f32_e32 v36, 1.0, v34
	v_rcp_f32_e32 v36, v36
	v_mul_f32_e32 v32, 0xbe38aa3b, v32
	v_min_f32_e32 v32, 0x42e60000, v32
	v_exp_f32_e32 v32, v32
	v_mul_f32_e32 v34, v34, v36
	v_cndmask_b32_e64 v40, 1.0, v34, s[66:67]
	v_cndmask_b32_e64 v78, 0, v36, s[66:67]
	v_cndmask_b32_e32 v34, v34, v40, vcc
	v_cndmask_b32_e32 v36, v36, v78, vcc
	v_mul_f32_e32 v36, v36, v35
	v_mul_f32_e32 v34, v34, v35
	v_add_f32_e32 v35, 1.0, v33
	v_rcp_f32_e32 v35, v35
	s_nop 0
	v_mul_f32_e32 v33, v33, v35
	v_cndmask_b32_e64 v40, 1.0, v33, s[68:69]
	v_cndmask_b32_e64 v78, 0, v35, s[68:69]
	v_cndmask_b32_e32 v33, v33, v40, vcc
	v_cndmask_b32_e32 v35, v35, v78, vcc
	v_mul_f32_e32 v35, v35, v34
	v_mul_f32_e32 v33, v33, v34
	v_add_f32_e32 v34, 1.0, v32
	v_rcp_f32_e32 v34, v34
	s_nop 0
	v_mul_f32_e32 v32, v32, v34
	v_cndmask_b32_e64 v40, 1.0, v32, s[70:71]
	v_cndmask_b32_e64 v78, 0, v34, s[70:71]
	v_cndmask_b32_e32 v32, v32, v40, vcc
	v_cndmask_b32_e32 v34, v34, v78, vcc
	v_mul_f32_e32 v78, v32, v33
	ds_bpermute_b32 v79, v69, v78
	v_mul_f32_e32 v34, v34, v33
	s_waitcnt lgkmcnt(0)
	v_mul_f32_e32 v32, v75, v79
	v_cndmask_b32_e64 v40, v75, v32, s[38:39]
	v_mul_f32_e32 v32, v40, v34
	v_mul_f32_e32 v33, v40, v35
	v_cvt_pk_bf16_f32 v32, v32, v33
	v_mul_f32_e32 v33, v40, v36
	v_mul_f32_e32 v34, v40, v37
	v_cvt_pk_bf16_f32 v33, v33, v34
	v_mul_f32_e32 v34, v40, v38
	v_mul_f32_e32 v35, v40, v39
	v_cvt_pk_bf16_f32 v34, v34, v35
	v_mul_f32_e32 v35, v40, v77
	v_mul_f32_e32 v36, v40, v41
	v_cvt_pk_bf16_f32 v35, v35, v36
	v_mul_f32_e32 v36, v40, v42
	v_mul_f32_e32 v37, v40, v43
	v_cvt_pk_bf16_f32 v36, v36, v37
	v_mul_f32_e32 v37, v40, v44
	v_mul_f32_e32 v38, v40, v45
	v_cvt_pk_bf16_f32 v37, v37, v38
	v_mul_f32_e32 v38, v40, v71
	v_mul_f32_e32 v39, v40, v73
	v_pk_mul_f32 v[40:41], v[40:41], v[46:47] op_sel_hi:[0,1]
	v_cvt_pk_bf16_f32 v38, v38, v39
	v_cvt_pk_bf16_f32 v39, v40, v41
	v_mul_f32_e32 v40, v75, v78
	v_mul_f32_e32 v75, v40, v79
	ds_read_b64_tr_b16 v[40:41], v74
	ds_read_b64_tr_b16 v[42:43], v74 offset:576
	ds_read_b64_tr_b16 v[44:45], v74 offset:64
	ds_read_b64_tr_b16 v[46:47], v74 offset:640
	ds_read_b64_tr_b16 v[78:79], v74 offset:1152
	ds_read_b64_tr_b16 v[80:81], v74 offset:1728
	ds_read_b64_tr_b16 v[82:83], v74 offset:1216
	ds_read_b64_tr_b16 v[84:85], v74 offset:1792
	s_waitcnt lgkmcnt(6)
	v_mfma_f32_32x32x16_bf16 v[0:15], v[32:35], v[40:43], v[0:15]
	v_cmp_gt_f32_e32 vcc, s19, v75
	s_cmp_lg_u64 vcc, exec
	s_cselect_b64 s[20:21], -1, 0
	s_cmp_lg_u32 s17, s18
	s_waitcnt lgkmcnt(0)
	s_cselect_b64 s[24:25], -1, 0
	s_and_b64 s[20:21], s[24:25], s[20:21]
	s_waitcnt lgkmcnt(4)
	v_mfma_f32_32x32x16_bf16 v[16:31], v[32:35], v[44:47], v[16:31]
	s_add_i32 s18, s18, 1
	s_sub_i32 s12, s12, 32
	s_and_b64 vcc, exec, s[20:21]
	s_waitcnt lgkmcnt(2)
	v_mfma_f32_32x32x16_bf16 v[0:15], v[36:39], v[78:81], v[0:15]
	s_waitcnt lgkmcnt(0)
	v_mfma_f32_32x32x16_bf16 v[16:31], v[36:39], v[82:85], v[16:31]
	s_cbranch_vccnz .Lmy_sb_lean
	s_branch .Lmy_sb_exit
.Lmy_sb_lean:
	s_add_u32 s19, s8, s12
	v_or_b32_e32 v32, s19, v66
	v_mov_b64_e32 v[36:37], s[88:89]
	s_addc_u32 s24, s9, 0
	v_mad_u64_u32 v[32:33], s[20:21], v32, s10, v[36:37]
	v_mad_i32_i24 v33, s24, v241, v33
	v_lshl_add_u64 v[32:33], v[32:33], 0, s[26:27]
	v_mov_b32_e32 v71, v48
	v_lshl_add_u64 v[32:33], v[32:33], 0, v[70:71]
	s_mov_b64 s[20:21], 0x1b80
	v_lshl_add_u64 v[38:39], v[32:33], 0, s[20:21]
	v_add_co_u32_e32 v32, vcc, s16, v32
	v_mov_b32_e32 v73, v48
	s_nop 0
	v_addc_co_u32_e32 v33, vcc, 0, v33, vcc
	global_load_dwordx4 v[32:35], v[32:33], off offset:2944
	s_nop 0
	global_load_dwordx4 v[78:81], v[38:39], off offset:32
	global_load_dwordx4 v[82:85], v[38:39], off offset:64
	global_load_dwordx4 v[86:89], v[38:39], off offset:96
	v_or_b32_e32 v38, s19, v68
	v_mad_u64_u32 v[36:37], s[20:21], v38, s10, v[36:37]
	v_mad_i32_i24 v37, s24, v241, v37
	v_lshl_add_u64 v[36:37], v[36:37], 0, s[26:27]
	v_lshl_add_u64 v[90:91], v[36:37], 0, v[72:73]
	v_add_co_u32_e32 v36, vcc, s16, v90
	s_mov_b32 s19, 0x13000
	s_nop 0
	v_addc_co_u32_e32 v37, vcc, 0, v91, vcc
	v_add_co_u32_e32 v40, vcc, s19, v90
	s_mov_b32 s19, 0x25000
	s_nop 0
	v_addc_co_u32_e32 v41, vcc, 0, v91, vcc
	v_add_co_u32_e32 v44, vcc, s19, v90
	global_load_dwordx4 v[36:39], v[36:37], off offset:3968
	s_nop 0
	v_addc_co_u32_e32 v45, vcc, 0, v91, vcc
	s_mov_b32 s19, 0x37000
	global_load_dwordx4 v[40:43], v[40:41], off offset:3968
	v_add_co_u32_e32 v90, vcc, s19, v90
	global_load_dwordx4 v[44:47], v[44:45], off offset:3968
	s_nop 0
	v_addc_co_u32_e32 v91, vcc, 0, v91, vcc
	global_load_dwordx4 v[90:93], v[90:91], off offset:3968
	s_mov_b32 s19, 0xda24260
	s_waitcnt vmcnt(3)
	ds_write_b128 v76, v[36:39]
	s_waitcnt vmcnt(2)
	ds_write_b128 v76, v[40:43] offset:1152
	s_waitcnt vmcnt(1)
	ds_write_b128 v76, v[44:47] offset:2304
	s_waitcnt vmcnt(0)
	ds_write_b128 v76, v[90:93] offset:3456
	v_mfma_f32_32x32x16_bf16 v[32:47], v[32:35], v[58:61], 0
	s_waitcnt lgkmcnt(0)
	v_mfma_f32_32x32x16_bf16 v[32:47], v[78:81], v[50:53], v[32:47]
	v_mfma_f32_32x32x16_bf16 v[32:47], v[82:85], v[54:57], v[32:47]
	v_mfma_f32_32x32x16_bf16 v[32:47], v[86:89], v[62:65], v[32:47]
	s_nop 11
	v_mul_f32_e32 v47, 0xbe38aa3b, v47
	v_min_f32_e32 v47, 0x42e60000, v47
	v_exp_f32_e32 v47, v47
	v_mul_f32_e32 v46, 0xbe38aa3b, v46
	v_min_f32_e32 v46, 0x42e60000, v46
	v_exp_f32_e32 v46, v46
	v_add_f32_e32 v71, 1.0, v47
	v_rcp_f32_e32 v71, v71
	v_mul_f32_e32 v45, 0xbe38aa3b, v45
	v_min_f32_e32 v45, 0x42e60000, v45
	v_exp_f32_e32 v45, v45
	v_mul_f32_e32 v47, v47, v71
	v_mov_b32_e32 v73, v47
	v_mov_b32_e32 v47, v71
	v_add_f32_e32 v71, 1.0, v46
	v_rcp_f32_e32 v71, v71
	v_mul_f32_e32 v44, 0xbe38aa3b, v44
	v_min_f32_e32 v44, 0x42e60000, v44
	v_exp_f32_e32 v44, v44
	v_mul_f32_e32 v46, v46, v71
	v_mov_b32_e32 v77, v46
	v_mov_b32_e32 v46, v71
	v_mul_f32_e32 v46, v46, v73
	v_mul_f32_e32 v71, v73, v77
	v_add_f32_e32 v73, 1.0, v45
	v_rcp_f32_e32 v73, v73
	v_mul_f32_e32 v43, 0xbe38aa3b, v43
	v_min_f32_e32 v43, 0x42e60000, v43
	v_exp_f32_e32 v43, v43
	v_mul_f32_e32 v45, v45, v73
	v_mul_f32_e32 v73, v73, v71
	v_mul_f32_e32 v45, v45, v71
	v_add_f32_e32 v71, 1.0, v44
	v_rcp_f32_e32 v71, v71
	v_mul_f32_e32 v42, 0xbe38aa3b, v42
	v_min_f32_e32 v42, 0x42e60000, v42
	v_exp_f32_e32 v42, v42
	v_mul_f32_e32 v44, v44, v71
	v_mul_f32_e32 v71, v71, v45
	v_mul_f32_e32 v44, v44, v45
	v_add_f32_e32 v45, 1.0, v43
	v_rcp_f32_e32 v45, v45
	v_mul_f32_e32 v41, 0xbe38aa3b, v41
	v_min_f32_e32 v41, 0x42e60000, v41
	v_exp_f32_e32 v41, v41
	v_mul_f32_e32 v43, v43, v45
	v_mul_f32_e32 v45, v45, v44
	v_mul_f32_e32 v43, v43, v44
	v_add_f32_e32 v44, 1.0, v42
	v_rcp_f32_e32 v44, v44
	v_mul_f32_e32 v40, 0xbe38aa3b, v40
	v_min_f32_e32 v40, 0x42e60000, v40
	v_exp_f32_e32 v40, v40
	v_mul_f32_e32 v42, v42, v44
	v_mul_f32_e32 v44, v44, v43
	v_mul_f32_e32 v42, v42, v43
	v_add_f32_e32 v43, 1.0, v41
	v_rcp_f32_e32 v43, v43
	v_mul_f32_e32 v39, 0xbe38aa3b, v39
	v_min_f32_e32 v39, 0x42e60000, v39
	v_exp_f32_e32 v39, v39
	v_mul_f32_e32 v41, v41, v43
	v_mul_f32_e32 v43, v43, v42
	v_mul_f32_e32 v41, v41, v42
	v_add_f32_e32 v42, 1.0, v40
	v_rcp_f32_e32 v42, v42
	v_mul_f32_e32 v38, 0xbe38aa3b, v38
	v_min_f32_e32 v38, 0x42e60000, v38
	v_exp_f32_e32 v38, v38
	v_mul_f32_e32 v40, v40, v42
	v_mul_f32_e32 v42, v42, v41
	v_mul_f32_e32 v40, v40, v41
	v_add_f32_e32 v41, 1.0, v39
	v_rcp_f32_e32 v41, v41
	v_mul_f32_e32 v37, 0xbe38aa3b, v37
	v_min_f32_e32 v37, 0x42e60000, v37
	v_exp_f32_e32 v37, v37
	v_mul_f32_e32 v39, v39, v41
	v_mul_f32_e32 v41, v41, v40
	v_mul_f32_e32 v39, v39, v40
	v_add_f32_e32 v40, 1.0, v38
	v_rcp_f32_e32 v40, v40
	v_mul_f32_e32 v36, 0xbe38aa3b, v36
	v_min_f32_e32 v36, 0x42e60000, v36
	v_exp_f32_e32 v36, v36
	v_mul_f32_e32 v38, v38, v40
	v_mul_f32_e32 v77, v40, v39
	v_mul_f32_e32 v38, v38, v39
	v_add_f32_e32 v39, 1.0, v37
	v_rcp_f32_e32 v39, v39
	v_mul_f32_e32 v35, 0xbe38aa3b, v35
	v_min_f32_e32 v35, 0x42e60000, v35
	v_exp_f32_e32 v35, v35
	v_mul_f32_e32 v37, v37, v39
	v_mul_f32_e32 v39, v39, v38
	v_mul_f32_e32 v37, v37, v38
	v_add_f32_e32 v38, 1.0, v36
	v_rcp_f32_e32 v38, v38
	v_mul_f32_e32 v34, 0xbe38aa3b, v34
	v_min_f32_e32 v34, 0x42e60000, v34
	v_exp_f32_e32 v34, v34
	v_mul_f32_e32 v36, v36, v38
	v_mul_f32_e32 v38, v38, v37
	v_mul_f32_e32 v36, v36, v37
	v_add_f32_e32 v37, 1.0, v35
	v_rcp_f32_e32 v37, v37
	v_mul_f32_e32 v33, 0xbe38aa3b, v33
	v_min_f32_e32 v33, 0x42e60000, v33
	v_exp_f32_e32 v33, v33
	v_mul_f32_e32 v35, v35, v37
	v_mul_f32_e32 v37, v37, v36
	v_mul_f32_e32 v35, v35, v36
	v_add_f32_e32 v36, 1.0, v34
	v_rcp_f32_e32 v36, v36
	v_mul_f32_e32 v32, 0xbe38aa3b, v32
	v_min_f32_e32 v32, 0x42e60000, v32
	v_exp_f32_e32 v32, v32
	v_mul_f32_e32 v34, v34, v36
	v_mul_f32_e32 v36, v36, v35
	v_mul_f32_e32 v34, v34, v35
	v_add_f32_e32 v35, 1.0, v33
	v_rcp_f32_e32 v35, v35
	s_nop 0
	v_mul_f32_e32 v33, v33, v35
	v_mul_f32_e32 v35, v35, v34
	v_mul_f32_e32 v33, v33, v34
	v_add_f32_e32 v34, 1.0, v32
	v_rcp_f32_e32 v34, v34
	s_nop 0
	v_mul_f32_e32 v32, v32, v34
	v_mul_f32_e32 v78, v32, v33
	ds_bpermute_b32 v79, v69, v78
	v_mul_f32_e32 v34, v34, v33
	s_waitcnt lgkmcnt(0)
	v_mul_f32_e32 v32, v75, v79
	v_cndmask_b32_e64 v40, v75, v32, s[38:39]
	v_mul_f32_e32 v32, v40, v34
	v_mul_f32_e32 v33, v40, v35
	v_cvt_pk_bf16_f32 v32, v32, v33
	v_mul_f32_e32 v33, v40, v36
	v_mul_f32_e32 v34, v40, v37
	v_cvt_pk_bf16_f32 v33, v33, v34
	v_mul_f32_e32 v34, v40, v38
	v_mul_f32_e32 v35, v40, v39
	v_cvt_pk_bf16_f32 v34, v34, v35
	v_mul_f32_e32 v35, v40, v77
	v_mul_f32_e32 v36, v40, v41
	v_cvt_pk_bf16_f32 v35, v35, v36
	v_mul_f32_e32 v36, v40, v42
	v_mul_f32_e32 v37, v40, v43
	v_cvt_pk_bf16_f32 v36, v36, v37
	v_mul_f32_e32 v37, v40, v44
	v_mul_f32_e32 v38, v40, v45
	v_cvt_pk_bf16_f32 v37, v37, v38
	v_mul_f32_e32 v38, v40, v71
	v_mul_f32_e32 v39, v40, v73
	v_pk_mul_f32 v[40:41], v[40:41], v[46:47] op_sel_hi:[0,1]
	v_cvt_pk_bf16_f32 v38, v38, v39
	v_cvt_pk_bf16_f32 v39, v40, v41
	v_mul_f32_e32 v40, v75, v78
	v_mul_f32_e32 v75, v40, v79
	ds_read_b64_tr_b16 v[40:41], v74
	ds_read_b64_tr_b16 v[42:43], v74 offset:576
	ds_read_b64_tr_b16 v[44:45], v74 offset:64
	ds_read_b64_tr_b16 v[46:47], v74 offset:640
	ds_read_b64_tr_b16 v[78:79], v74 offset:1152
	ds_read_b64_tr_b16 v[80:81], v74 offset:1728
	ds_read_b64_tr_b16 v[82:83], v74 offset:1216
	ds_read_b64_tr_b16 v[84:85], v74 offset:1792
	s_waitcnt lgkmcnt(6)
	v_mfma_f32_32x32x16_bf16 v[0:15], v[32:35], v[40:43], v[0:15]
	v_cmp_gt_f32_e32 vcc, s19, v75
	s_cmp_lg_u64 vcc, exec
	s_cselect_b64 s[20:21], -1, 0
	s_cmp_lg_u32 s17, s18
	s_waitcnt lgkmcnt(0)
	s_cselect_b64 s[24:25], -1, 0
	s_and_b64 s[20:21], s[24:25], s[20:21]
	s_waitcnt lgkmcnt(4)
	v_mfma_f32_32x32x16_bf16 v[16:31], v[32:35], v[44:47], v[16:31]
	s_add_i32 s18, s18, 1
	s_sub_i32 s12, s12, 32
	s_and_b64 vcc, exec, s[20:21]
	s_waitcnt lgkmcnt(2)
	v_mfma_f32_32x32x16_bf16 v[0:15], v[36:39], v[78:81], v[0:15]
	s_waitcnt lgkmcnt(0)
	v_mfma_f32_32x32x16_bf16 v[16:31], v[36:39], v[82:85], v[16:31]
	s_cbranch_vccnz .Lmy_sb_lean
.Lmy_sb_exit:
	v_readlane_b32 s24, v255, 30
	v_readlane_b32 s25, v255, 31
	v_readlane_b32 s26, v255, 18
	s_mov_b32 s69, 0x22000
	s_mov_b32 s68, 0x19000
	s_mov_b32 s71, 0x1d000
	s_mov_b32 s70, 0x1f000
	s_mov_b32 s66, s28
	s_mov_b32 s67, s29
	s_branch .LBB0_539

.LBB0_552:
	s_waitcnt vmcnt(1)
	v_mfma_f32_16x16x32_bf16 v[80:83], v[62:65], v[28:31], 0
	v_mul_hi_u32 v96, s25, v76
	v_mul_lo_u32 v98, s21, v96
	v_mul_lo_u32 v97, s24, v96
	s_waitcnt vmcnt(0)
	v_mfma_f32_16x16x32_bf16 v[80:83], v[58:61], v[24:27], v[80:83]
	v_mfma_f32_16x16x32_bf16 v[84:87], v[62:65], v[20:23], 0
	s_nop 6
	v_max_f32_e32 v88, 0, v80
	v_max_f32_e32 v90, 0, v81
	v_max_f32_e32 v92, 0, v82
	v_max_f32_e32 v94, 0, v83
	v_mfma_f32_16x16x32_bf16 v[80:83], v[58:61], v[16:19], v[84:87]
	v_mfma_f32_16x16x32_bf16 v[84:87], v[62:65], v[12:15], 0
	v_mfma_f32_16x16x32_bf16 v[62:65], v[62:65], v[4:7], 0
	s_nop 5
	v_max_f32_e32 v89, 0, v80
	v_max_f32_e32 v91, 0, v81
	v_max_f32_e32 v93, 0, v82
	v_max_f32_e32 v95, 0, v83
	v_mfma_f32_16x16x32_bf16 v[80:83], v[58:61], v[8:11], v[84:87]
	v_mul_f32_e64 v88, v66, v88
	v_mul_f32_e64 v89, v67, v89
	v_pk_mul_f32 v[90:91], v[66:67], v[90:91]
	v_pk_mul_f32 v[92:93], v[66:67], v[92:93]
	v_mfma_f32_16x16x32_bf16 v[58:61], v[58:61], v[0:3], v[62:65]
	v_mul_f32_e64 v94, v66, v94
	v_mul_f32_e64 v95, v67, v95
	s_nop 0
	v_max_f32_e32 v84, 0, v81
	v_max_f32_e32 v82, 0, v82
	v_max_f32_e32 v80, 0, v80
	v_max_f32_e32 v86, 0, v83
	v_max_f32_e32 v81, 0, v58
	v_pk_mul_f32 v[62:63], v[68:69], v[80:81]
	v_max_f32_e32 v85, 0, v59
	v_mov_b32_e32 v80, v90
	v_mov_b32_e32 v81, v88
	v_pk_mul_f32 v[58:59], v[68:69], v[84:85]
	v_max_f32_e32 v83, 0, v60
	v_pk_add_f32 v[80:81], v[80:81], 0 op_sel_hi:[1,0]
	v_mov_b32_e32 v88, v91
	v_pk_mul_f32 v[64:65], v[68:69], v[82:83]
	v_pk_add_f32 v[80:81], v[80:81], v[88:89]
	v_mov_b32_e32 v82, v58
	v_mov_b32_e32 v83, v62
	v_pk_add_f32 v[80:81], v[80:81], v[82:83]
	v_mov_b32_e32 v62, v59
	v_pk_add_f32 v[58:59], v[80:81], v[62:63]
	v_cmp_lt_i32_e32 vcc, -1, v59
	v_max_f32_e32 v87, 0, v61
	v_pk_mul_f32 v[60:61], v[68:69], v[86:87]
	v_cndmask_b32_e32 v62, -1, v242, vcc
	v_cmp_lt_i32_e32 vcc, -1, v58
	v_xor_b32_e32 v80, v62, v59
	v_mov_b32_e32 v62, v60
	v_cndmask_b32_e32 v59, -1, v242, vcc
	v_xor_b32_e32 v81, v59, v58
	v_mov_b32_e32 v58, v94
	v_mov_b32_e32 v59, v92
	v_pk_add_f32 v[58:59], v[58:59], 0 op_sel_hi:[1,0]
	v_mov_b32_e32 v92, v95
	v_pk_add_f32 v[58:59], v[58:59], v[92:93]
	v_mov_b32_e32 v63, v64
	v_pk_add_f32 v[58:59], v[58:59], v[62:63]
	v_mov_b32_e32 v64, v61
	v_pk_add_f32 v[58:59], v[58:59], v[64:65]
	v_add_u32_e32 v62, v74, v96
	v_cmp_lt_i32_e32 vcc, -1, v59
	s_nop 1
	v_cndmask_b32_e32 v60, -1, v242, vcc
	v_cmp_lt_i32_e32 vcc, -1, v58
	v_xor_b32_e32 v60, v60, v59
	s_nop 0
	v_cndmask_b32_e32 v59, -1, v242, vcc
	v_xor_b32_e32 v61, v59, v58
	v_mad_u64_u32 v[58:59], s[28:29], s26, v96, v[70:71]
	v_and_b32_e32 v59, 0x7ff, v58
	v_add_u32_e32 v58, 32, v58
	v_lshl_add_u32 v59, v59, 2, v75
	v_and_b32_e32 v58, 0x7ff, v58
	ds_write_b32 v59, v80
	v_lshl_add_u32 v58, v58, 2, v75
	v_add3_u32 v59, v98, s21, -2
	ds_write_b32 v58, v81
	v_add3_u32 v58, v76, v97, 2
	v_cmp_eq_u32_e32 vcc, v59, v76
	s_nop 1
	v_cndmask_b32_e64 v58, v58, 0, vcc
	v_cndmask_b32_e64 v59, 0, 1, vcc
	v_addc_co_u32_e32 v63, vcc, v74, v96, vcc
	v_lshl_add_u32 v63, v58, 5, v63
	v_and_b32_e32 v63, 0x7ff, v63
	v_lshl_add_u32 v63, v63, 2, v75
	v_add_u32_e32 v58, 1, v58
	ds_write_b32 v63, v60
	v_lshlrev_b32_e32 v60, 5, v58
	v_cmp_eq_u32_e32 vcc, s21, v58
	s_nop 1
	v_cndmask_b32_e64 v58, v60, 0, vcc
	v_addc_co_u32_e32 v59, vcc, v62, v59, vcc
	v_add_u32_e32 v58, v59, v58
	v_and_b32_e32 v58, 0x7ff, v58
	v_lshl_add_u32 v58, v58, 2, v75
	s_andn2_b64 vcc, exec, s[38:39]
	ds_write_b32 v58, v61
	s_cbranch_vccnz .LBB0_555
	v_mfma_f32_16x16x32_bf16 v[58:61], v[44:47], v[28:31], 0
	v_mul_hi_u32 v96, s25, v79
	v_mul_lo_u32 v62, s21, v96
	v_add_u32_e32 v98, s21, v62
	v_mfma_f32_16x16x32_bf16 v[58:61], v[54:57], v[24:27], v[58:61]
	v_mul_lo_u32 v97, s24, v96
	v_mfma_f32_16x16x32_bf16 v[62:65], v[44:47], v[20:23], 0
	s_nop 5
	v_max_f32_e32 v80, 0, v58
	v_max_f32_e32 v84, 0, v60
	v_max_f32_e32 v82, 0, v59
	v_max_f32_e32 v86, 0, v61
	v_mfma_f32_16x16x32_bf16 v[58:61], v[54:57], v[16:19], v[62:65]
	v_mfma_f32_16x16x32_bf16 v[62:65], v[44:47], v[12:15], 0
	s_nop 6
	v_max_f32_e32 v81, 0, v58
	v_max_f32_e32 v83, 0, v59
	v_max_f32_e32 v85, 0, v60
	v_max_f32_e32 v87, 0, v61
	v_mfma_f32_16x16x32_bf16 v[58:61], v[54:57], v[8:11], v[62:65]
	v_mul_f32_e64 v80, v66, v80
	v_mul_f32_e64 v81, v67, v81
	v_pk_mul_f32 v[82:83], v[66:67], v[82:83]
	v_pk_mul_f32 v[84:85], v[66:67], v[84:85]
	v_mfma_f32_16x16x32_bf16 v[62:65], v[44:47], v[4:7], 0
	v_mul_f32_e64 v86, v66, v86
	v_mul_f32_e64 v87, v67, v87
	s_nop 0
	v_max_f32_e32 v88, 0, v58
	v_max_f32_e32 v90, 0, v59
	v_max_f32_e32 v92, 0, v60
	v_max_f32_e32 v94, 0, v61
	v_mfma_f32_16x16x32_bf16 v[58:61], v[54:57], v[0:3], v[62:65]
	s_nop 7
	v_max_f32_e32 v89, 0, v58
	v_pk_mul_f32 v[62:63], v[68:69], v[88:89]
	v_max_f32_e32 v91, 0, v59
	v_mov_b32_e32 v88, v82
	v_mov_b32_e32 v89, v80
	v_pk_mul_f32 v[58:59], v[68:69], v[90:91]
	v_pk_add_f32 v[88:89], v[88:89], 0 op_sel_hi:[1,0]
	v_mov_b32_e32 v80, v83
	v_pk_add_f32 v[80:81], v[88:89], v[80:81]
	v_mov_b32_e32 v82, v58
	v_mov_b32_e32 v83, v62
	v_pk_add_f32 v[80:81], v[80:81], v[82:83]
	v_mov_b32_e32 v62, v59
	v_pk_add_f32 v[58:59], v[80:81], v[62:63]
	v_cmp_lt_i32_e32 vcc, -1, v59
	v_max_f32_e32 v93, 0, v60
	v_cndmask_b32_e32 v62, -1, v242, vcc
	v_cmp_lt_i32_e32 vcc, -1, v58
	v_xor_b32_e32 v80, v62, v59
	v_max_f32_e32 v95, 0, v61
	v_cndmask_b32_e32 v59, -1, v242, vcc
	v_xor_b32_e32 v81, v59, v58
	v_mov_b32_e32 v58, v86
	v_mov_b32_e32 v59, v84
	v_pk_mul_f32 v[64:65], v[68:69], v[92:93]
	v_pk_mul_f32 v[60:61], v[68:69], v[94:95]
	v_pk_add_f32 v[58:59], v[58:59], 0 op_sel_hi:[1,0]
	v_mov_b32_e32 v84, v87
	v_pk_add_f32 v[58:59], v[58:59], v[84:85]
	v_mov_b32_e32 v62, v60
	v_mov_b32_e32 v63, v64
	v_pk_add_f32 v[58:59], v[58:59], v[62:63]
	v_mov_b32_e32 v64, v61
	v_pk_add_f32 v[58:59], v[58:59], v[64:65]
	s_nop 0
	v_cmp_lt_i32_e32 vcc, -1, v59
	s_nop 1
	v_cndmask_b32_e32 v60, -1, v242, vcc
	v_cmp_lt_i32_e32 vcc, -1, v58
	v_xor_b32_e32 v60, v60, v59
	s_nop 0
	v_cndmask_b32_e32 v59, -1, v242, vcc
	v_xor_b32_e32 v61, v59, v58
	v_add_u32_e32 v58, 0x80, v76
	v_mul_hi_u32 v62, v58, s25
	v_mad_u64_u32 v[58:59], s[28:29], s26, v96, v[70:71]
	v_add_u32_e32 v59, 0x1000, v58
	v_and_b32_e32 v59, 0x7ff, v59
	v_add_u32_e32 v58, 0x1020, v58
	v_lshl_add_u32 v59, v59, 2, v75
	v_and_b32_e32 v58, 0x7ff, v58
	ds_write_b32 v59, v80
	v_lshl_add_u32 v58, v58, 2, v75
	s_movk_i32 s28, 0x82
	v_add_u32_e32 v59, 0xffffff7e, v98
	ds_write_b32 v58, v81
	v_add3_u32 v58, v76, v97, s28
	v_cmp_eq_u32_e32 vcc, v59, v76
	v_add_u32_e32 v63, v74, v62
	s_nop 0
	v_cndmask_b32_e64 v58, v58, 0, vcc
	v_cndmask_b32_e64 v59, 0, 1, vcc
	v_addc_co_u32_e32 v62, vcc, v74, v62, vcc
	v_lshl_add_u32 v62, v58, 5, v62
	v_and_b32_e32 v62, 0x7ff, v62
	v_lshl_add_u32 v62, v62, 2, v75
	v_add_u32_e32 v58, 1, v58
	ds_write_b32 v62, v60
	v_lshlrev_b32_e32 v60, 5, v58
	v_cmp_eq_u32_e32 vcc, s21, v58
	s_nop 1
	v_cndmask_b32_e64 v58, v60, 0, vcc
	v_addc_co_u32_e32 v59, vcc, v63, v59, vcc
	v_add_u32_e32 v58, v59, v58
	v_and_b32_e32 v58, 0x7ff, v58
	v_lshl_add_u32 v58, v58, 2, v75
	ds_write_b32 v58, v61
	s_andn2_b64 vcc, exec, s[8:9]
	s_cbranch_vccz .LBB0_556

.LBB0_556:
	v_mfma_f32_16x16x32_bf16 v[58:61], v[40:43], v[28:31], 0
	v_mul_hi_u32 v96, s25, v78
	v_mul_lo_u32 v62, s21, v96
	v_add_u32_e32 v98, s21, v62
	v_mfma_f32_16x16x32_bf16 v[58:61], v[50:53], v[24:27], v[58:61]
	v_mul_lo_u32 v97, s24, v96
	v_mfma_f32_16x16x32_bf16 v[62:65], v[40:43], v[20:23], 0
	s_nop 5
	v_max_f32_e32 v80, 0, v58
	v_max_f32_e32 v84, 0, v60
	v_max_f32_e32 v82, 0, v59
	v_max_f32_e32 v86, 0, v61
	v_mfma_f32_16x16x32_bf16 v[58:61], v[50:53], v[16:19], v[62:65]
	v_mfma_f32_16x16x32_bf16 v[62:65], v[40:43], v[12:15], 0
	s_nop 6
	v_max_f32_e32 v81, 0, v58
	v_max_f32_e32 v83, 0, v59
	v_max_f32_e32 v85, 0, v60
	v_max_f32_e32 v87, 0, v61
	v_mfma_f32_16x16x32_bf16 v[58:61], v[50:53], v[8:11], v[62:65]
	v_mul_f32_e64 v80, v66, v80
	v_mul_f32_e64 v81, v67, v81
	v_pk_mul_f32 v[82:83], v[66:67], v[82:83]
	v_pk_mul_f32 v[84:85], v[66:67], v[84:85]
	v_mfma_f32_16x16x32_bf16 v[62:65], v[40:43], v[4:7], 0
	v_mul_f32_e64 v86, v66, v86
	v_mul_f32_e64 v87, v67, v87
	s_nop 0
	v_max_f32_e32 v88, 0, v58
	v_max_f32_e32 v90, 0, v59
	v_max_f32_e32 v92, 0, v60
	v_max_f32_e32 v94, 0, v61
	v_mfma_f32_16x16x32_bf16 v[58:61], v[50:53], v[0:3], v[62:65]
	s_nop 7
	v_max_f32_e32 v89, 0, v58
	v_pk_mul_f32 v[62:63], v[68:69], v[88:89]
	v_max_f32_e32 v91, 0, v59
	v_mov_b32_e32 v88, v82
	v_mov_b32_e32 v89, v80
	v_pk_mul_f32 v[58:59], v[68:69], v[90:91]
	v_pk_add_f32 v[88:89], v[88:89], 0 op_sel_hi:[1,0]
	v_mov_b32_e32 v80, v83
	v_pk_add_f32 v[80:81], v[88:89], v[80:81]
	v_mov_b32_e32 v82, v58
	v_mov_b32_e32 v83, v62
	v_pk_add_f32 v[80:81], v[80:81], v[82:83]
	v_mov_b32_e32 v62, v59
	v_pk_add_f32 v[58:59], v[80:81], v[62:63]
	v_cmp_lt_i32_e32 vcc, -1, v59
	v_max_f32_e32 v93, 0, v60
	v_cndmask_b32_e32 v62, -1, v242, vcc
	v_cmp_lt_i32_e32 vcc, -1, v58
	v_xor_b32_e32 v80, v62, v59
	v_max_f32_e32 v95, 0, v61
	v_cndmask_b32_e32 v59, -1, v242, vcc
	v_xor_b32_e32 v81, v59, v58
	v_mov_b32_e32 v58, v86
	v_mov_b32_e32 v59, v84
	v_pk_mul_f32 v[64:65], v[68:69], v[92:93]
	v_pk_mul_f32 v[60:61], v[68:69], v[94:95]
	v_pk_add_f32 v[58:59], v[58:59], 0 op_sel_hi:[1,0]
	v_mov_b32_e32 v84, v87
	v_pk_add_f32 v[58:59], v[58:59], v[84:85]
	v_mov_b32_e32 v62, v60
	v_mov_b32_e32 v63, v64
	v_pk_add_f32 v[58:59], v[58:59], v[62:63]
	v_mov_b32_e32 v64, v61
	v_pk_add_f32 v[58:59], v[58:59], v[64:65]
	s_nop 0
	v_cmp_lt_i32_e32 vcc, -1, v59
	s_nop 1
	v_cndmask_b32_e32 v60, -1, v242, vcc
	v_cmp_lt_i32_e32 vcc, -1, v58
	v_xor_b32_e32 v60, v60, v59
	s_nop 0
	v_cndmask_b32_e32 v59, -1, v242, vcc
	v_xor_b32_e32 v61, v59, v58
	v_add_u32_e32 v58, 0x100, v76
	v_mul_hi_u32 v62, v58, s25
	v_mad_u64_u32 v[58:59], s[8:9], s26, v96, v[70:71]
	v_add_u32_e32 v59, 0x2000, v58
	v_and_b32_e32 v59, 0x7ff, v59
	v_add_u32_e32 v58, 0x2020, v58
	v_lshl_add_u32 v59, v59, 2, v75
	v_and_b32_e32 v58, 0x7ff, v58
	ds_write_b32 v59, v80
	v_lshl_add_u32 v58, v58, 2, v75
	s_movk_i32 s8, 0x102
	v_add_u32_e32 v59, 0xfffffefe, v98
	ds_write_b32 v58, v81
	v_add3_u32 v58, v76, v97, s8
	v_cmp_eq_u32_e32 vcc, v59, v76
	v_add_u32_e32 v63, v74, v62
	s_nop 0
	v_cndmask_b32_e64 v58, v58, 0, vcc
	v_cndmask_b32_e64 v59, 0, 1, vcc
	v_addc_co_u32_e32 v62, vcc, v74, v62, vcc
	v_lshl_add_u32 v62, v58, 5, v62
	v_and_b32_e32 v62, 0x7ff, v62
	v_lshl_add_u32 v62, v62, 2, v75
	v_add_u32_e32 v58, 1, v58
	ds_write_b32 v62, v60
	v_lshlrev_b32_e32 v60, 5, v58
	v_cmp_eq_u32_e32 vcc, s21, v58
	s_nop 1
	v_cndmask_b32_e64 v58, v60, 0, vcc
	v_addc_co_u32_e32 v59, vcc, v63, v59, vcc
	v_add_u32_e32 v58, v59, v58
	v_and_b32_e32 v58, 0x7ff, v58
	v_lshl_add_u32 v58, v58, 2, v75
	ds_write_b32 v58, v61
	s_andn2_b64 vcc, exec, s[6:7]
	s_cbranch_vccnz .LBB0_545
.LBB0_557:
	v_mfma_f32_16x16x32_bf16 v[58:61], v[32:35], v[28:31], 0
	v_mul_hi_u32 v96, s25, v77
	v_mul_lo_u32 v62, s21, v96
	v_add_u32_e32 v98, s21, v62
	v_mfma_f32_16x16x32_bf16 v[58:61], v[36:39], v[24:27], v[58:61]
	v_mul_lo_u32 v97, s24, v96
	v_mfma_f32_16x16x32_bf16 v[62:65], v[32:35], v[20:23], 0
	s_nop 5
	v_max_f32_e32 v80, 0, v58
	v_max_f32_e32 v84, 0, v60
	v_max_f32_e32 v82, 0, v59
	v_max_f32_e32 v86, 0, v61
	v_mfma_f32_16x16x32_bf16 v[58:61], v[36:39], v[16:19], v[62:65]
	v_mfma_f32_16x16x32_bf16 v[62:65], v[32:35], v[12:15], 0
	s_nop 6
	v_max_f32_e32 v81, 0, v58
	v_max_f32_e32 v83, 0, v59
	v_max_f32_e32 v85, 0, v60
	v_max_f32_e32 v87, 0, v61
	v_mfma_f32_16x16x32_bf16 v[58:61], v[36:39], v[8:11], v[62:65]
	v_mul_f32_e64 v80, v66, v80
	v_mul_f32_e64 v81, v67, v81
	v_pk_mul_f32 v[82:83], v[66:67], v[82:83]
	v_pk_mul_f32 v[84:85], v[66:67], v[84:85]
	v_mfma_f32_16x16x32_bf16 v[62:65], v[32:35], v[4:7], 0
	v_mul_f32_e64 v86, v66, v86
	v_mul_f32_e64 v87, v67, v87
	s_nop 0
	v_max_f32_e32 v88, 0, v58
	v_max_f32_e32 v90, 0, v59
	v_max_f32_e32 v92, 0, v60
	v_max_f32_e32 v94, 0, v61
	v_mfma_f32_16x16x32_bf16 v[58:61], v[36:39], v[0:3], v[62:65]
	s_nop 7
	v_max_f32_e32 v89, 0, v58
	v_pk_mul_f32 v[62:63], v[68:69], v[88:89]
	v_max_f32_e32 v91, 0, v59
	v_mov_b32_e32 v88, v82
	v_mov_b32_e32 v89, v80
	v_pk_mul_f32 v[58:59], v[68:69], v[90:91]
	v_pk_add_f32 v[88:89], v[88:89], 0 op_sel_hi:[1,0]
	v_mov_b32_e32 v80, v83
	v_pk_add_f32 v[80:81], v[88:89], v[80:81]
	v_mov_b32_e32 v82, v58
	v_mov_b32_e32 v83, v62
	v_pk_add_f32 v[80:81], v[80:81], v[82:83]
	v_mov_b32_e32 v62, v59
	v_pk_add_f32 v[58:59], v[80:81], v[62:63]
	v_cmp_lt_i32_e32 vcc, -1, v59
	v_max_f32_e32 v93, 0, v60
	v_cndmask_b32_e32 v62, -1, v242, vcc
	v_cmp_lt_i32_e32 vcc, -1, v58
	v_xor_b32_e32 v80, v62, v59
	v_max_f32_e32 v95, 0, v61
	v_cndmask_b32_e32 v59, -1, v242, vcc
	v_xor_b32_e32 v81, v59, v58
	v_mov_b32_e32 v58, v86
	v_mov_b32_e32 v59, v84
	v_pk_mul_f32 v[64:65], v[68:69], v[92:93]
	v_pk_mul_f32 v[60:61], v[68:69], v[94:95]
	v_pk_add_f32 v[58:59], v[58:59], 0 op_sel_hi:[1,0]
	v_mov_b32_e32 v84, v87
	v_pk_add_f32 v[58:59], v[58:59], v[84:85]
	v_mov_b32_e32 v62, v60
	v_mov_b32_e32 v63, v64
	v_pk_add_f32 v[58:59], v[58:59], v[62:63]
	v_mov_b32_e32 v64, v61
	v_pk_add_f32 v[58:59], v[58:59], v[64:65]
	s_nop 0
	v_cmp_lt_i32_e32 vcc, -1, v59
	s_nop 1
	v_cndmask_b32_e32 v60, -1, v242, vcc
	v_cmp_lt_i32_e32 vcc, -1, v58
	v_xor_b32_e32 v60, v60, v59
	s_nop 0
	v_cndmask_b32_e32 v59, -1, v242, vcc
	v_xor_b32_e32 v61, v59, v58
	v_add_u32_e32 v58, 0x180, v76
	v_mul_hi_u32 v62, v58, s25
	v_mad_u64_u32 v[58:59], s[6:7], s26, v96, v[70:71]
	v_add_u32_e32 v59, 0x3000, v58
	v_and_b32_e32 v59, 0x7ff, v59
	v_add_u32_e32 v58, 0x3020, v58
	v_lshl_add_u32 v59, v59, 2, v75
	v_and_b32_e32 v58, 0x7ff, v58
	ds_write_b32 v59, v80
	v_lshl_add_u32 v58, v58, 2, v75
	s_movk_i32 s6, 0x182
	v_add_u32_e32 v59, 0xfffffe7e, v98
	ds_write_b32 v58, v81
	v_add3_u32 v58, v76, v97, s6
	v_cmp_eq_u32_e32 vcc, v59, v76
	v_add_u32_e32 v63, v74, v62
	s_nop 0
	v_cndmask_b32_e64 v58, v58, 0, vcc
	v_cndmask_b32_e64 v59, 0, 1, vcc
	v_addc_co_u32_e32 v62, vcc, v74, v62, vcc
	v_lshl_add_u32 v62, v58, 5, v62
	v_and_b32_e32 v62, 0x7ff, v62
	v_lshl_add_u32 v62, v62, 2, v75
	v_add_u32_e32 v58, 1, v58
	ds_write_b32 v62, v60
	v_lshlrev_b32_e32 v60, 5, v58
	v_cmp_eq_u32_e32 vcc, s21, v58
	s_nop 1
	v_cndmask_b32_e64 v58, v60, 0, vcc
	v_addc_co_u32_e32 v59, vcc, v63, v59, vcc
	v_add_u32_e32 v58, v59, v58
	v_and_b32_e32 v58, 0x7ff, v58
	v_lshl_add_u32 v58, v58, 2, v75
	ds_write_b32 v58, v61
	s_branch .LBB0_545
